# GEMM K-loops: the back-to-back s_setprio 0 / s_setprio 1 pair in the middle of each 32-MFMA burst removed (12 pairs), heads re-aligned, on top of combo14
# speedup vs baseline: 1.0098x; 1.0001x over previous
; #define PG8_STAGE(bufoff, gbase, voff) do { _Pragma("unroll") for (int _i = 0; _i < 2; ++_i) \
;         __builtin_amdgcn_global_load_lds((const unsigned*)((const char*)(gbase) + (voff)[_i]), (PG8_LAS unsigned*)(lds + (bufoff) + ldsw + _i * 8192), 16, 0, 0); } while (0)
; #define PG8_LDA(dst, b, h) do { _Pragma("unroll") for (int m = 0; m < 4; ++m) _Pragma("unroll") for (int k = 0; k < 2; ++k) dst[m][k] = *(const PG8_LAS bf16x8*)(lds + PG8_SA(b, h) + aoff + m * 2048 + k * 1024); } while (0)
; #define PG8_LDB(dst, b, h) do { _Pragma("unroll") for (int n = 0; n < 2; ++n) _Pragma("unroll") for (int k = 0; k < 2; ++k) dst[n][k] = *(const PG8_LAS bf16x8*)(lds + PG8_SB(b, h) + boff + n * 2048 + k * 1024); } while (0)
; #define PG8_MMA(ai, bj, At, Bt) do { __builtin_amdgcn_s_setprio(1); _Pragma("unroll") for (int m = 0; m < 4; ++m) _Pragma("unroll") for (int n = 0; n < 2; ++n) _Pragma("unroll") for (int k = 0; k < 2; ++k) \
;         acc[ai][bj][m][n] = __builtin_amdgcn_mfma_f32_16x16x32_bf16(Bt[n][k], At[m][k], acc[ai][bj][m][n], 0, 0, 0); __builtin_amdgcn_s_setprio(0); } while (0)
; #define PG8_WAIT_V(n) asm volatile("s_waitcnt vmcnt(" #n ")" ::: "memory")
; #define PG8_WAIT_L(n) asm volatile("s_waitcnt lgkmcnt(" #n ")" ::: "memory")
; template <class Epi, class Sched, bool ALIGN_EPI = false, bool SP2 = false>
; __device__ __forceinline__ void gemm_phase(PG8_LAS unsigned char* lds, const Gemm g, const Sched& S, const Epi& E) {
;     ...
;             const bool last = (t == nt - 2);
;             const char* a1 = cA + (size_t)(t + 1) * kstep;
;             const char* a2 = last ? nA : cA + (size_t)(t + 2) * kstep; const char* b2 = last ? nB : cB + (size_t)(t + 2) * kstep;
;             const char* a3 = a2 + kstep; const char* b3 = b2 + kstep;
;             if (last && has_next) S.a_ready(nxt);
;             if constexpr (SP2) {
;             PG8_LDB(B0, 0, 0); PG8_LDB(B1, 0, 1); PG8_SCHED; PG8_LDA(At, 0, 0); PG8_STAGE(PG8_SA(1, 1), a1 + hstep, voffA);
;             PG8_WAIT_V(8); PG8_WAIT_L(0); PG8_BAR; PG8_MMA(0, 0, At, B0); PG8_MMA(0, 1, At, B1); PG8_BAR; PG8_SCHED;
;             PG8_LDA(At, 0, 1); PG8_STAGE(PG8_SB(0, 0), b2, voffB); PG8_STAGE(PG8_SB(0, 1), b2 + hstep, voffB); PG8_STAGE(PG8_SA(0, 0), a2, voffA);
;             PG8_WAIT_V(8); PG8_WAIT_L(0); PG8_BAR; PG8_MMA(1, 0, At, B0); PG8_MMA(1, 1, At, B1); PG8_BAR; PG8_SCHED;
.LBB0_102:
	ds_read_b128 v[154:157], v159
	ds_read_b128 v[162:165], v159 offset:1024
	ds_read_b128 v[166:169], v159 offset:2048
	ds_read_b128 v[170:173], v159 offset:3072
	ds_read_b128 v[174:177], v160
	ds_read_b128 v[178:181], v160 offset:1024
	ds_read_b128 v[184:187], v160 offset:2048
	ds_read_b128 v[188:191], v160 offset:3072
	s_add_u32 s26, s24, 0xfff00080
	s_addc_u32 s27, s25, -1
	s_cmp_eq_u32 s50, 60
	s_cselect_b32 s29, s17, s27
	s_cselect_b32 s28, s23, s26
	s_cselect_b32 s27, s15, s49
	s_cselect_b32 s26, s46, s47
	s_nop 0
	s_add_i32 m0, s34, 0xc000
	ds_read_b128 v[192:195], v161
	ds_read_b128 v[196:199], v161 offset:1024
	ds_read_b128 v[200:203], v161 offset:2048
	ds_read_b128 v[204:207], v161 offset:3072
	ds_read_b128 v[208:211], v161 offset:4096
	ds_read_b128 v[212:215], v161 offset:5120
	ds_read_b128 v[216:219], v161 offset:6144
	ds_read_b128 v[220:223], v161 offset:7168
	global_load_lds_dwordx4 v146, s[24:25]
	s_nop 0
	s_add_i32 m0, s34, 0xe000
	s_nop 0
	global_load_lds_dwordx4 v148, s[24:25]
	s_waitcnt vmcnt(8)
	s_waitcnt lgkmcnt(0)
	s_barrier
	s_setprio 1
	s_waitcnt lgkmcnt(0)
	v_mfma_f32_16x16x32_bf16 v[126:129], v[154:157], v[192:195], v[126:129]
	v_mfma_f32_16x16x32_bf16 v[122:125], v[166:169], v[192:195], v[122:125]
	v_mfma_f32_16x16x32_bf16 v[110:113], v[154:157], v[200:203], v[110:113]
	v_mfma_f32_16x16x32_bf16 v[106:109], v[166:169], v[200:203], v[106:109]
	v_mfma_f32_16x16x32_bf16 v[98:101], v[154:157], v[208:211], v[98:101]
	v_mfma_f32_16x16x32_bf16 v[90:93], v[166:169], v[208:211], v[90:93]
	v_mfma_f32_16x16x32_bf16 v[82:85], v[154:157], v[216:219], v[82:85]
	v_mfma_f32_16x16x32_bf16 v[74:77], v[166:169], v[216:219], v[74:77]
	v_mfma_f32_16x16x32_bf16 v[126:129], v[162:165], v[196:199], v[126:129]
	v_mfma_f32_16x16x32_bf16 v[122:125], v[170:173], v[196:199], v[122:125]
	v_mfma_f32_16x16x32_bf16 v[110:113], v[162:165], v[204:207], v[110:113]
	v_mfma_f32_16x16x32_bf16 v[106:109], v[170:173], v[204:207], v[106:109]
	v_mfma_f32_16x16x32_bf16 v[98:101], v[162:165], v[212:215], v[98:101]
	v_mfma_f32_16x16x32_bf16 v[90:93], v[170:173], v[212:215], v[90:93]
	v_mfma_f32_16x16x32_bf16 v[82:85], v[162:165], v[220:223], v[82:85]
	v_mfma_f32_16x16x32_bf16 v[74:77], v[170:173], v[220:223], v[74:77]
	v_mfma_f32_16x16x32_bf16 v[118:121], v[174:177], v[192:195], v[118:121]
	v_mfma_f32_16x16x32_bf16 v[114:117], v[184:187], v[192:195], v[114:117]
	v_mfma_f32_16x16x32_bf16 v[102:105], v[174:177], v[200:203], v[102:105]
	v_mfma_f32_16x16x32_bf16 v[94:97], v[184:187], v[200:203], v[94:97]
	v_mfma_f32_16x16x32_bf16 v[86:89], v[174:177], v[208:211], v[86:89]
	v_mfma_f32_16x16x32_bf16 v[78:81], v[184:187], v[208:211], v[78:81]
	v_mfma_f32_16x16x32_bf16 v[70:73], v[174:177], v[216:219], v[70:73]
	v_mfma_f32_16x16x32_bf16 v[66:69], v[184:187], v[216:219], v[66:69]
	v_mfma_f32_16x16x32_bf16 v[118:121], v[178:181], v[196:199], v[118:121]
	v_mfma_f32_16x16x32_bf16 v[114:117], v[188:191], v[196:199], v[114:117]
	v_mfma_f32_16x16x32_bf16 v[102:105], v[178:181], v[204:207], v[102:105]
	v_mfma_f32_16x16x32_bf16 v[94:97], v[188:191], v[204:207], v[94:97]
	v_mfma_f32_16x16x32_bf16 v[86:89], v[178:181], v[212:215], v[86:89]
	v_mfma_f32_16x16x32_bf16 v[78:81], v[188:191], v[212:215], v[78:81]
	v_mfma_f32_16x16x32_bf16 v[70:73], v[178:181], v[220:223], v[70:73]
	v_mfma_f32_16x16x32_bf16 v[66:69], v[188:191], v[220:223], v[66:69]
	s_setprio 0
	s_barrier
	s_add_i32 s51, s42, s30
	s_nop 0
	s_mov_b32 m0, s51
	ds_read_b128 v[192:195], v161 offset:16384
	ds_read_b128 v[196:199], v161 offset:17408
	ds_read_b128 v[200:203], v161 offset:18432
	ds_read_b128 v[204:207], v161 offset:19456
	ds_read_b128 v[208:211], v161 offset:20480
	ds_read_b128 v[212:215], v161 offset:21504
	ds_read_b128 v[216:219], v161 offset:22528
	ds_read_b128 v[220:223], v161 offset:23552
	global_load_lds_dwordx4 v140, s[26:27]
	s_add_i32 m0, s51, 0x2000
	s_add_u32 s52, s26, 0x100000
	s_nop 0
	s_addc_u32 s53, s27, 0
	s_add_i32 s51, s43, s30
	global_load_lds_dwordx4 v136, s[26:27]
	s_nop 0
	s_mov_b32 m0, s51
	s_add_u32 s58, s28, s6
	s_addc_u32 s59, s29, s7
	global_load_lds_dwordx4 v140, s[52:53]
	s_nop 0
	s_add_i32 m0, s51, 0x2000
	s_nop 0
	global_load_lds_dwordx4 v136, s[52:53]
	s_nop 0
	s_mov_b32 m0, s34
	s_nop 0
	global_load_lds_dwordx4 v142, s[28:29]
	s_mov_b32 m0, s35
	s_nop 0
	global_load_lds_dwordx4 v138, s[28:29]
	s_waitcnt vmcnt(8)
	s_waitcnt lgkmcnt(0)
	s_barrier
	s_setprio 1
	s_waitcnt lgkmcnt(0)
	v_mfma_f32_16x16x32_bf16 v[62:65], v[154:157], v[192:195], v[62:65]
	v_mfma_f32_16x16x32_bf16 v[58:61], v[166:169], v[192:195], v[58:61]
	v_mfma_f32_16x16x32_bf16 v[50:53], v[154:157], v[200:203], v[50:53]
	v_mfma_f32_16x16x32_bf16 v[42:45], v[166:169], v[200:203], v[42:45]
	v_mfma_f32_16x16x32_bf16 v[34:37], v[154:157], v[208:211], v[34:37]
	v_mfma_f32_16x16x32_bf16 v[26:29], v[166:169], v[208:211], v[26:29]
	v_mfma_f32_16x16x32_bf16 v[18:21], v[154:157], v[216:219], v[18:21]
	v_mfma_f32_16x16x32_bf16 v[10:13], v[166:169], v[216:219], v[10:13]
	v_mfma_f32_16x16x32_bf16 v[62:65], v[162:165], v[196:199], v[62:65]
	v_mfma_f32_16x16x32_bf16 v[58:61], v[170:173], v[196:199], v[58:61]
	v_mfma_f32_16x16x32_bf16 v[50:53], v[162:165], v[204:207], v[50:53]
	v_mfma_f32_16x16x32_bf16 v[42:45], v[170:173], v[204:207], v[42:45]
	v_mfma_f32_16x16x32_bf16 v[34:37], v[162:165], v[212:215], v[34:37]
	v_mfma_f32_16x16x32_bf16 v[26:29], v[170:173], v[212:215], v[26:29]
	v_mfma_f32_16x16x32_bf16 v[18:21], v[162:165], v[220:223], v[18:21]
	v_mfma_f32_16x16x32_bf16 v[10:13], v[170:173], v[220:223], v[10:13]
	v_mfma_f32_16x16x32_bf16 v[54:57], v[174:177], v[192:195], v[54:57]
	v_mfma_f32_16x16x32_bf16 v[46:49], v[184:187], v[192:195], v[46:49]
	v_mfma_f32_16x16x32_bf16 v[38:41], v[174:177], v[200:203], v[38:41]
	v_mfma_f32_16x16x32_bf16 v[30:33], v[184:187], v[200:203], v[30:33]
	v_mfma_f32_16x16x32_bf16 v[22:25], v[174:177], v[208:211], v[22:25]
	v_mfma_f32_16x16x32_bf16 v[14:17], v[184:187], v[208:211], v[14:17]
	v_mfma_f32_16x16x32_bf16 v[6:9], v[174:177], v[216:219], v[6:9]
	v_mfma_f32_16x16x32_bf16 v[2:5], v[184:187], v[216:219], v[2:5]
	v_mfma_f32_16x16x32_bf16 v[54:57], v[178:181], v[196:199], v[54:57]
	v_mfma_f32_16x16x32_bf16 v[46:49], v[188:191], v[196:199], v[46:49]
	v_mfma_f32_16x16x32_bf16 v[38:41], v[178:181], v[204:207], v[38:41]
	v_mfma_f32_16x16x32_bf16 v[30:33], v[188:191], v[204:207], v[30:33]
	v_mfma_f32_16x16x32_bf16 v[22:25], v[178:181], v[212:215], v[22:25]
	v_mfma_f32_16x16x32_bf16 v[14:17], v[188:191], v[212:215], v[14:17]
	v_mfma_f32_16x16x32_bf16 v[6:9], v[178:181], v[220:223], v[6:9]
	v_mfma_f32_16x16x32_bf16 v[2:5], v[188:191], v[220:223], v[2:5]
	s_setprio 0
	s_barrier
; #define PG8_STAGE(bufoff, gbase, voff) do { _Pragma("unroll") for (int _i = 0; _i < 2; ++_i) \
;         __builtin_amdgcn_global_load_lds((const unsigned*)((const char*)(gbase) + (voff)[_i]), (PG8_LAS unsigned*)(lds + (bufoff) + ldsw + _i * 8192), 16, 0, 0); } while (0)
; #define PG8_LDA(dst, b, h) do { _Pragma("unroll") for (int m = 0; m < 4; ++m) _Pragma("unroll") for (int k = 0; k < 2; ++k) dst[m][k] = *(const PG8_LAS bf16x8*)(lds + PG8_SA(b, h) + aoff + m * 2048 + k * 1024); } while (0)
; #define PG8_LDB(dst, b, h) do { _Pragma("unroll") for (int n = 0; n < 2; ++n) _Pragma("unroll") for (int k = 0; k < 2; ++k) dst[n][k] = *(const PG8_LAS bf16x8*)(lds + PG8_SB(b, h) + boff + n * 2048 + k * 1024); } while (0)
; #define PG8_MMA(ai, bj, At, Bt) do { __builtin_amdgcn_s_setprio(1); _Pragma("unroll") for (int m = 0; m < 4; ++m) _Pragma("unroll") for (int n = 0; n < 2; ++n) _Pragma("unroll") for (int k = 0; k < 2; ++k) \
;         acc[ai][bj][m][n] = __builtin_amdgcn_mfma_f32_16x16x32_bf16(Bt[n][k], At[m][k], acc[ai][bj][m][n], 0, 0, 0); __builtin_amdgcn_s_setprio(0); } while (0)
; #define PG8_WAIT_V(n) asm volatile("s_waitcnt vmcnt(" #n ")" ::: "memory")
; #define PG8_WAIT_L(n) asm volatile("s_waitcnt lgkmcnt(" #n ")" ::: "memory")
; #define PG8_BAR __builtin_amdgcn_s_barrier()
; #define PG8_SCHED __builtin_amdgcn_sched_barrier(0)
; template <class Epi, class Sched, bool ALIGN_EPI = false, bool SP2 = false>
; __device__ __forceinline__ void gemm_phase(PG8_LAS unsigned char* lds, const Gemm g, const Sched& S, const Epi& E) {
;     ...
;             PG8_LDB(B0, 1, 0); PG8_LDB(B1, 1, 1); PG8_SCHED; PG8_LDA(At, 1, 0); PG8_STAGE(PG8_SA(0, 1), a2 + hstep, voffA);
;             PG8_WAIT_V(8); PG8_WAIT_L(0); PG8_BAR; PG8_MMA(0, 0, At, B0); PG8_MMA(0, 1, At, B1); PG8_BAR; PG8_SCHED;
;             PG8_LDA(At, 1, 1); PG8_STAGE(PG8_SB(1, 0), b3, voffB); PG8_STAGE(PG8_SB(1, 1), b3 + hstep, voffB); PG8_STAGE(PG8_SA(1, 0), a3, voffA);
;             PG8_WAIT_V(8); PG8_WAIT_L(0); PG8_BAR; PG8_MMA(1, 0, At, B0); PG8_MMA(1, 1, At, B1); PG8_BAR; PG8_SCHED;
;     ...
;         if constexpr (ALIGN_EPI) { if (wr == 0) PG8_BAR; }
	s_add_i32 s51, 0, 0x18000
	v_add_u32_e32 v144, s51, v133
	s_add_i32 s52, 0, 0x1c000
	ds_read_b128 v[154:157], v144
	ds_read_b128 v[162:165], v144 offset:1024
	ds_read_b128 v[166:169], v144 offset:2048
	ds_read_b128 v[170:173], v144 offset:3072
	v_add_u32_e32 v144, s52, v133
	ds_read_b128 v[174:177], v144
	ds_read_b128 v[178:181], v144 offset:1024
	ds_read_b128 v[184:187], v144 offset:2048
	ds_read_b128 v[188:191], v144 offset:3072
	s_add_u32 s28, s28, 0x100000
	s_addc_u32 s29, s29, 0
	s_mov_b32 m0, s36
	s_nop 0
	ds_read_b128 v[192:195], v161 offset:32768
	ds_read_b128 v[196:199], v161 offset:33792
	ds_read_b128 v[200:203], v161 offset:34816
	ds_read_b128 v[204:207], v161 offset:35840
	ds_read_b128 v[208:211], v161 offset:36864
	ds_read_b128 v[212:215], v161 offset:37888
	ds_read_b128 v[216:219], v161 offset:38912
	ds_read_b128 v[220:223], v161 offset:39936
	global_load_lds_dwordx4 v142, s[28:29]
	s_nop 0
	s_mov_b32 m0, s37
	s_nop 0
	global_load_lds_dwordx4 v138, s[28:29]
	s_waitcnt vmcnt(8)
	s_waitcnt lgkmcnt(0)
	s_barrier
	s_setprio 1
	s_waitcnt lgkmcnt(0)
	v_mfma_f32_16x16x32_bf16 v[126:129], v[154:157], v[192:195], v[126:129]
	v_mfma_f32_16x16x32_bf16 v[122:125], v[166:169], v[192:195], v[122:125]
	v_mfma_f32_16x16x32_bf16 v[110:113], v[154:157], v[200:203], v[110:113]
	v_mfma_f32_16x16x32_bf16 v[106:109], v[166:169], v[200:203], v[106:109]
	v_mfma_f32_16x16x32_bf16 v[98:101], v[154:157], v[208:211], v[98:101]
	v_mfma_f32_16x16x32_bf16 v[90:93], v[166:169], v[208:211], v[90:93]
	v_mfma_f32_16x16x32_bf16 v[82:85], v[154:157], v[216:219], v[82:85]
	v_mfma_f32_16x16x32_bf16 v[74:77], v[166:169], v[216:219], v[74:77]
	v_mfma_f32_16x16x32_bf16 v[126:129], v[162:165], v[196:199], v[126:129]
	v_mfma_f32_16x16x32_bf16 v[122:125], v[170:173], v[196:199], v[122:125]
	v_mfma_f32_16x16x32_bf16 v[110:113], v[162:165], v[204:207], v[110:113]
	v_mfma_f32_16x16x32_bf16 v[106:109], v[170:173], v[204:207], v[106:109]
	v_mfma_f32_16x16x32_bf16 v[98:101], v[162:165], v[212:215], v[98:101]
	v_mfma_f32_16x16x32_bf16 v[90:93], v[170:173], v[212:215], v[90:93]
	v_mfma_f32_16x16x32_bf16 v[82:85], v[162:165], v[220:223], v[82:85]
	v_mfma_f32_16x16x32_bf16 v[74:77], v[170:173], v[220:223], v[74:77]
	v_mfma_f32_16x16x32_bf16 v[118:121], v[174:177], v[192:195], v[118:121]
	v_mfma_f32_16x16x32_bf16 v[114:117], v[184:187], v[192:195], v[114:117]
	v_mfma_f32_16x16x32_bf16 v[102:105], v[174:177], v[200:203], v[102:105]
	v_mfma_f32_16x16x32_bf16 v[94:97], v[184:187], v[200:203], v[94:97]
	v_mfma_f32_16x16x32_bf16 v[86:89], v[174:177], v[208:211], v[86:89]
	v_mfma_f32_16x16x32_bf16 v[78:81], v[184:187], v[208:211], v[78:81]
	v_mfma_f32_16x16x32_bf16 v[70:73], v[174:177], v[216:219], v[70:73]
	v_mfma_f32_16x16x32_bf16 v[66:69], v[184:187], v[216:219], v[66:69]
	v_mfma_f32_16x16x32_bf16 v[118:121], v[178:181], v[196:199], v[118:121]
	v_mfma_f32_16x16x32_bf16 v[114:117], v[188:191], v[196:199], v[114:117]
	v_mfma_f32_16x16x32_bf16 v[102:105], v[178:181], v[204:207], v[102:105]
	v_mfma_f32_16x16x32_bf16 v[94:97], v[188:191], v[204:207], v[94:97]
	v_mfma_f32_16x16x32_bf16 v[86:89], v[178:181], v[212:215], v[86:89]
	v_mfma_f32_16x16x32_bf16 v[78:81], v[188:191], v[212:215], v[78:81]
	v_mfma_f32_16x16x32_bf16 v[70:73], v[178:181], v[220:223], v[70:73]
	v_mfma_f32_16x16x32_bf16 v[66:69], v[188:191], v[220:223], v[66:69]
	s_setprio 0
	s_barrier
	s_add_i32 s28, s51, s30
	s_add_u32 s54, s26, s6
	s_addc_u32 s55, s27, s7
	s_mov_b32 m0, s28
	ds_read_b128 v[192:195], v161 offset:49152
	ds_read_b128 v[196:199], v161 offset:50176
	ds_read_b128 v[200:203], v161 offset:51200
	ds_read_b128 v[204:207], v161 offset:52224
	ds_read_b128 v[208:211], v161 offset:53248
	ds_read_b128 v[212:215], v161 offset:54272
	ds_read_b128 v[216:219], v161 offset:55296
	ds_read_b128 v[220:223], v161 offset:56320
	global_load_lds_dwordx4 v140, s[54:55]
	s_add_i32 m0, s28, 0x2000
	s_add_u32 s26, s26, 0x100080
	s_nop 0
	s_addc_u32 s27, s27, 0
	s_add_i32 s28, s52, s30
	global_load_lds_dwordx4 v136, s[54:55]
	s_nop 0
	s_mov_b32 m0, s28
	s_nop 0
	global_load_lds_dwordx4 v140, s[26:27]
	s_nop 0
	s_add_i32 m0, s28, 0x2000
	s_nop 0
	global_load_lds_dwordx4 v136, s[26:27]
	s_nop 0
	s_mov_b32 m0, s39
	s_nop 0
	global_load_lds_dwordx4 v142, s[58:59]
	s_nop 0
	s_mov_b32 m0, s40
	s_nop 0
	global_load_lds_dwordx4 v138, s[58:59]
	s_waitcnt vmcnt(8)
	s_waitcnt lgkmcnt(0)
	s_barrier
	s_setprio 1
	s_waitcnt lgkmcnt(0)
	v_mfma_f32_16x16x32_bf16 v[62:65], v[154:157], v[192:195], v[62:65]
	v_mfma_f32_16x16x32_bf16 v[58:61], v[166:169], v[192:195], v[58:61]
	v_mfma_f32_16x16x32_bf16 v[50:53], v[154:157], v[200:203], v[50:53]
	v_mfma_f32_16x16x32_bf16 v[42:45], v[166:169], v[200:203], v[42:45]
	v_mfma_f32_16x16x32_bf16 v[34:37], v[154:157], v[208:211], v[34:37]
	v_mfma_f32_16x16x32_bf16 v[26:29], v[166:169], v[208:211], v[26:29]
	v_mfma_f32_16x16x32_bf16 v[18:21], v[154:157], v[216:219], v[18:21]
	v_mfma_f32_16x16x32_bf16 v[10:13], v[166:169], v[216:219], v[10:13]
	v_mfma_f32_16x16x32_bf16 v[62:65], v[162:165], v[196:199], v[62:65]
	v_mfma_f32_16x16x32_bf16 v[58:61], v[170:173], v[196:199], v[58:61]
	v_mfma_f32_16x16x32_bf16 v[50:53], v[162:165], v[204:207], v[50:53]
	v_mfma_f32_16x16x32_bf16 v[42:45], v[170:173], v[204:207], v[42:45]
	v_mfma_f32_16x16x32_bf16 v[34:37], v[162:165], v[212:215], v[34:37]
	v_mfma_f32_16x16x32_bf16 v[26:29], v[170:173], v[212:215], v[26:29]
	v_mfma_f32_16x16x32_bf16 v[18:21], v[162:165], v[220:223], v[18:21]
	v_mfma_f32_16x16x32_bf16 v[10:13], v[170:173], v[220:223], v[10:13]
	v_mfma_f32_16x16x32_bf16 v[54:57], v[174:177], v[192:195], v[54:57]
	v_mfma_f32_16x16x32_bf16 v[46:49], v[184:187], v[192:195], v[46:49]
	v_mfma_f32_16x16x32_bf16 v[38:41], v[174:177], v[200:203], v[38:41]
	v_mfma_f32_16x16x32_bf16 v[30:33], v[184:187], v[200:203], v[30:33]
	v_mfma_f32_16x16x32_bf16 v[22:25], v[174:177], v[208:211], v[22:25]
	v_mfma_f32_16x16x32_bf16 v[14:17], v[184:187], v[208:211], v[14:17]
	v_mfma_f32_16x16x32_bf16 v[6:9], v[174:177], v[216:219], v[6:9]
	v_mfma_f32_16x16x32_bf16 v[2:5], v[184:187], v[216:219], v[2:5]
	v_mfma_f32_16x16x32_bf16 v[54:57], v[178:181], v[196:199], v[54:57]
	v_mfma_f32_16x16x32_bf16 v[46:49], v[188:191], v[196:199], v[46:49]
	v_mfma_f32_16x16x32_bf16 v[38:41], v[178:181], v[204:207], v[38:41]
	v_mfma_f32_16x16x32_bf16 v[30:33], v[188:191], v[204:207], v[30:33]
	v_mfma_f32_16x16x32_bf16 v[22:25], v[178:181], v[212:215], v[22:25]
	v_mfma_f32_16x16x32_bf16 v[14:17], v[188:191], v[212:215], v[14:17]
	v_mfma_f32_16x16x32_bf16 v[6:9], v[178:181], v[220:223], v[6:9]
	v_mfma_f32_16x16x32_bf16 v[2:5], v[188:191], v[220:223], v[2:5]
	s_setprio 0
	s_barrier
	s_add_i32 s50, s50, 2
	s_add_u32 s24, s24, 0x100
	s_addc_u32 s25, s25, 0
	s_add_u32 s47, s47, 0x100
	s_addc_u32 s49, s49, 0
	s_cmp_gt_u32 s50, 61
	s_cbranch_scc0 .LBB0_102
	s_and_b64 vcc, exec, s[12:13]
	s_cbranch_vccz .LBB0_105
	s_barrier

; #define PG8_STAGE(bufoff, gbase, voff) do { _Pragma("unroll") for (int _i = 0; _i < 2; ++_i) \
;         __builtin_amdgcn_global_load_lds((const unsigned*)((const char*)(gbase) + (voff)[_i]), (PG8_LAS unsigned*)(lds + (bufoff) + ldsw + _i * 8192), 16, 0, 0); } while (0)
; #define PG8_LDA(dst, b, h) do { _Pragma("unroll") for (int m = 0; m < 4; ++m) _Pragma("unroll") for (int k = 0; k < 2; ++k) dst[m][k] = *(const PG8_LAS bf16x8*)(lds + PG8_SA(b, h) + aoff + m * 2048 + k * 1024); } while (0)
; #define PG8_LDB(dst, b, h) do { _Pragma("unroll") for (int n = 0; n < 2; ++n) _Pragma("unroll") for (int k = 0; k < 2; ++k) dst[n][k] = *(const PG8_LAS bf16x8*)(lds + PG8_SB(b, h) + boff + n * 2048 + k * 1024); } while (0)
; #define PG8_MMA(ai, bj, At, Bt) do { __builtin_amdgcn_s_setprio(1); _Pragma("unroll") for (int m = 0; m < 4; ++m) _Pragma("unroll") for (int n = 0; n < 2; ++n) _Pragma("unroll") for (int k = 0; k < 2; ++k) \
;         acc[ai][bj][m][n] = __builtin_amdgcn_mfma_f32_16x16x32_bf16(Bt[n][k], At[m][k], acc[ai][bj][m][n], 0, 0, 0); __builtin_amdgcn_s_setprio(0); } while (0)
; #define PG8_WAIT_V(n) asm volatile("s_waitcnt vmcnt(" #n ")" ::: "memory")
; #define PG8_WAIT_L(n) asm volatile("s_waitcnt lgkmcnt(" #n ")" ::: "memory")
; template <class Epi, class Sched, bool ALIGN_EPI = false, bool SP2 = false>
; __device__ __forceinline__ void gemm_phase(PG8_LAS unsigned char* lds, const Gemm g, const Sched& S, const Epi& E) {
;     ...
;             const bool last = (t == nt - 2);
;             const char* a1 = cA + (size_t)(t + 1) * kstep;
;             const char* a2 = last ? nA : cA + (size_t)(t + 2) * kstep; const char* b2 = last ? nB : cB + (size_t)(t + 2) * kstep;
;             const char* a3 = a2 + kstep; const char* b3 = b2 + kstep;
;             if (last && has_next) S.a_ready(nxt);
;             if constexpr (SP2) {
;             PG8_LDB(B0, 0, 0); PG8_LDB(B1, 0, 1); PG8_SCHED; PG8_LDA(At, 0, 0); PG8_STAGE(PG8_SA(1, 1), a1 + hstep, voffA);
;             PG8_WAIT_V(8); PG8_WAIT_L(0); PG8_BAR; PG8_MMA(0, 0, At, B0); PG8_MMA(0, 1, At, B1); PG8_BAR; PG8_SCHED;
;             PG8_LDA(At, 0, 1); PG8_STAGE(PG8_SB(0, 0), b2, voffB); PG8_STAGE(PG8_SB(0, 1), b2 + hstep, voffB); PG8_STAGE(PG8_SA(0, 0), a2, voffA);
;             PG8_WAIT_V(8); PG8_WAIT_L(0); PG8_BAR; PG8_MMA(1, 0, At, B0); PG8_MMA(1, 1, At, B1); PG8_BAR; PG8_SCHED;
.LBB0_563:
	ds_read_b128 v[146:149], v154
	ds_read_b128 v[158:161], v154 offset:1024
	ds_read_b128 v[162:165], v154 offset:2048
	ds_read_b128 v[166:169], v154 offset:3072
	ds_read_b128 v[170:173], v155
	ds_read_b128 v[174:177], v155 offset:1024
	ds_read_b128 v[178:181], v155 offset:2048
	ds_read_b128 v[184:187], v155 offset:3072
	s_add_u32 s30, s28, 0xffe00080
	s_addc_u32 s31, s29, -1
	s_cmpk_eq_i32 s51, 0x7c
	s_cselect_b32 s35, s21, s31
	s_cselect_b32 s34, s47, s30
	s_cselect_b32 s31, s19, s50
	s_cselect_b32 s30, s48, s49
	s_nop 0
	s_add_i32 m0, s27, 0xc000
	ds_read_b128 v[188:191], v156
	ds_read_b128 v[192:195], v156 offset:1024
	ds_read_b128 v[196:199], v156 offset:2048
	ds_read_b128 v[200:203], v156 offset:3072
	ds_read_b128 v[204:207], v156 offset:4096
	ds_read_b128 v[208:211], v156 offset:5120
	ds_read_b128 v[212:215], v156 offset:6144
	ds_read_b128 v[216:219], v156 offset:7168
	global_load_lds_dwordx4 v138, s[28:29]
	s_nop 0
	s_add_i32 m0, s27, 0xe000
	s_nop 0
	global_load_lds_dwordx4 v140, s[28:29]
	s_waitcnt vmcnt(8)
	s_waitcnt lgkmcnt(0)
	s_barrier
	s_setprio 1
	s_waitcnt lgkmcnt(0)
	v_mfma_f32_16x16x32_bf16 v[126:129], v[146:149], v[188:191], v[126:129]
	v_mfma_f32_16x16x32_bf16 v[122:125], v[162:165], v[188:191], v[122:125]
	v_mfma_f32_16x16x32_bf16 v[110:113], v[146:149], v[196:199], v[110:113]
	v_mfma_f32_16x16x32_bf16 v[106:109], v[162:165], v[196:199], v[106:109]
	v_mfma_f32_16x16x32_bf16 v[94:97], v[146:149], v[204:207], v[94:97]
	v_mfma_f32_16x16x32_bf16 v[90:93], v[162:165], v[204:207], v[90:93]
	v_mfma_f32_16x16x32_bf16 v[78:81], v[146:149], v[212:215], v[78:81]
	v_mfma_f32_16x16x32_bf16 v[74:77], v[162:165], v[212:215], v[74:77]
	v_mfma_f32_16x16x32_bf16 v[126:129], v[158:161], v[192:195], v[126:129]
	v_mfma_f32_16x16x32_bf16 v[122:125], v[166:169], v[192:195], v[122:125]
	v_mfma_f32_16x16x32_bf16 v[110:113], v[158:161], v[200:203], v[110:113]
	v_mfma_f32_16x16x32_bf16 v[106:109], v[166:169], v[200:203], v[106:109]
	v_mfma_f32_16x16x32_bf16 v[94:97], v[158:161], v[208:211], v[94:97]
	v_mfma_f32_16x16x32_bf16 v[90:93], v[166:169], v[208:211], v[90:93]
	v_mfma_f32_16x16x32_bf16 v[78:81], v[158:161], v[216:219], v[78:81]
	v_mfma_f32_16x16x32_bf16 v[74:77], v[166:169], v[216:219], v[74:77]
	v_mfma_f32_16x16x32_bf16 v[118:121], v[170:173], v[188:191], v[118:121]
	v_mfma_f32_16x16x32_bf16 v[114:117], v[178:181], v[188:191], v[114:117]
	v_mfma_f32_16x16x32_bf16 v[102:105], v[170:173], v[196:199], v[102:105]
	v_mfma_f32_16x16x32_bf16 v[98:101], v[178:181], v[196:199], v[98:101]
	v_mfma_f32_16x16x32_bf16 v[86:89], v[170:173], v[204:207], v[86:89]
	v_mfma_f32_16x16x32_bf16 v[82:85], v[178:181], v[204:207], v[82:85]
	v_mfma_f32_16x16x32_bf16 v[70:73], v[170:173], v[212:215], v[70:73]
	v_mfma_f32_16x16x32_bf16 v[66:69], v[178:181], v[212:215], v[66:69]
	v_mfma_f32_16x16x32_bf16 v[118:121], v[174:177], v[192:195], v[118:121]
	v_mfma_f32_16x16x32_bf16 v[114:117], v[184:187], v[192:195], v[114:117]
	v_mfma_f32_16x16x32_bf16 v[102:105], v[174:177], v[200:203], v[102:105]
	v_mfma_f32_16x16x32_bf16 v[98:101], v[184:187], v[200:203], v[98:101]
	v_mfma_f32_16x16x32_bf16 v[86:89], v[174:177], v[208:211], v[86:89]
	v_mfma_f32_16x16x32_bf16 v[82:85], v[184:187], v[208:211], v[82:85]
	v_mfma_f32_16x16x32_bf16 v[70:73], v[174:177], v[216:219], v[70:73]
	v_mfma_f32_16x16x32_bf16 v[66:69], v[184:187], v[216:219], v[66:69]
	s_setprio 0
	s_barrier
	s_add_i32 s52, s44, s36
	s_nop 0
	s_mov_b32 m0, s52
	ds_read_b128 v[188:191], v156 offset:16384
	ds_read_b128 v[192:195], v156 offset:17408
	ds_read_b128 v[196:199], v156 offset:18432
	ds_read_b128 v[200:203], v156 offset:19456
	ds_read_b128 v[204:207], v156 offset:20480
	ds_read_b128 v[208:211], v156 offset:21504
	ds_read_b128 v[212:215], v156 offset:22528
	ds_read_b128 v[216:219], v156 offset:23552
	global_load_lds_dwordx4 v132, s[30:31]
	s_add_i32 m0, s52, 0x2000
	s_add_u32 s52, s30, 0x200000
	s_nop 0
	s_addc_u32 s53, s31, 0
	s_add_i32 s54, s45, s36
	global_load_lds_dwordx4 v136, s[30:31]
	s_nop 0
	s_mov_b32 m0, s54
	s_add_u32 s60, s34, s2
	s_addc_u32 s61, s35, s3
	global_load_lds_dwordx4 v132, s[52:53]
	s_nop 0
	s_add_i32 m0, s54, 0x2000
	s_nop 0
	global_load_lds_dwordx4 v136, s[52:53]
	s_nop 0
	s_mov_b32 m0, s27
	s_nop 0
	global_load_lds_dwordx4 v130, s[34:35]
	s_mov_b32 m0, s37
	s_nop 0
	global_load_lds_dwordx4 v134, s[34:35]
	s_waitcnt vmcnt(8)
	s_waitcnt lgkmcnt(0)
	s_barrier
	s_setprio 1
	s_waitcnt lgkmcnt(0)
	v_mfma_f32_16x16x32_bf16 v[62:65], v[146:149], v[188:191], v[62:65]
	v_mfma_f32_16x16x32_bf16 v[58:61], v[162:165], v[188:191], v[58:61]
	v_mfma_f32_16x16x32_bf16 v[46:49], v[146:149], v[196:199], v[46:49]
	v_mfma_f32_16x16x32_bf16 v[42:45], v[162:165], v[196:199], v[42:45]
	v_mfma_f32_16x16x32_bf16 v[30:33], v[146:149], v[204:207], v[30:33]
	v_mfma_f32_16x16x32_bf16 v[26:29], v[162:165], v[204:207], v[26:29]
	v_mfma_f32_16x16x32_bf16 v[14:17], v[146:149], v[212:215], v[14:17]
	v_mfma_f32_16x16x32_bf16 v[10:13], v[162:165], v[212:215], v[10:13]
	v_mfma_f32_16x16x32_bf16 v[62:65], v[158:161], v[192:195], v[62:65]
	v_mfma_f32_16x16x32_bf16 v[58:61], v[166:169], v[192:195], v[58:61]
	v_mfma_f32_16x16x32_bf16 v[46:49], v[158:161], v[200:203], v[46:49]
	v_mfma_f32_16x16x32_bf16 v[42:45], v[166:169], v[200:203], v[42:45]
	v_mfma_f32_16x16x32_bf16 v[30:33], v[158:161], v[208:211], v[30:33]
	v_mfma_f32_16x16x32_bf16 v[26:29], v[166:169], v[208:211], v[26:29]
	v_mfma_f32_16x16x32_bf16 v[14:17], v[158:161], v[216:219], v[14:17]
	v_mfma_f32_16x16x32_bf16 v[10:13], v[166:169], v[216:219], v[10:13]
	v_mfma_f32_16x16x32_bf16 v[54:57], v[170:173], v[188:191], v[54:57]
	v_mfma_f32_16x16x32_bf16 v[50:53], v[178:181], v[188:191], v[50:53]
	v_mfma_f32_16x16x32_bf16 v[38:41], v[170:173], v[196:199], v[38:41]
	v_mfma_f32_16x16x32_bf16 v[34:37], v[178:181], v[196:199], v[34:37]
	v_mfma_f32_16x16x32_bf16 v[22:25], v[170:173], v[204:207], v[22:25]
	v_mfma_f32_16x16x32_bf16 v[18:21], v[178:181], v[204:207], v[18:21]
	v_mfma_f32_16x16x32_bf16 v[6:9], v[170:173], v[212:215], v[6:9]
	v_mfma_f32_16x16x32_bf16 v[2:5], v[178:181], v[212:215], v[2:5]
	v_mfma_f32_16x16x32_bf16 v[54:57], v[174:177], v[192:195], v[54:57]
	v_mfma_f32_16x16x32_bf16 v[50:53], v[184:187], v[192:195], v[50:53]
	v_mfma_f32_16x16x32_bf16 v[38:41], v[174:177], v[200:203], v[38:41]
	v_mfma_f32_16x16x32_bf16 v[34:37], v[184:187], v[200:203], v[34:37]
	v_mfma_f32_16x16x32_bf16 v[22:25], v[174:177], v[208:211], v[22:25]
	v_mfma_f32_16x16x32_bf16 v[18:21], v[184:187], v[208:211], v[18:21]
	v_mfma_f32_16x16x32_bf16 v[6:9], v[174:177], v[216:219], v[6:9]
	v_mfma_f32_16x16x32_bf16 v[2:5], v[184:187], v[216:219], v[2:5]
	s_setprio 0
	s_barrier
; #define PG8_STAGE(bufoff, gbase, voff) do { _Pragma("unroll") for (int _i = 0; _i < 2; ++_i) \
;         __builtin_amdgcn_global_load_lds((const unsigned*)((const char*)(gbase) + (voff)[_i]), (PG8_LAS unsigned*)(lds + (bufoff) + ldsw + _i * 8192), 16, 0, 0); } while (0)
; #define PG8_LDA(dst, b, h) do { _Pragma("unroll") for (int m = 0; m < 4; ++m) _Pragma("unroll") for (int k = 0; k < 2; ++k) dst[m][k] = *(const PG8_LAS bf16x8*)(lds + PG8_SA(b, h) + aoff + m * 2048 + k * 1024); } while (0)
; #define PG8_LDB(dst, b, h) do { _Pragma("unroll") for (int n = 0; n < 2; ++n) _Pragma("unroll") for (int k = 0; k < 2; ++k) dst[n][k] = *(const PG8_LAS bf16x8*)(lds + PG8_SB(b, h) + boff + n * 2048 + k * 1024); } while (0)
; #define PG8_MMA(ai, bj, At, Bt) do { __builtin_amdgcn_s_setprio(1); _Pragma("unroll") for (int m = 0; m < 4; ++m) _Pragma("unroll") for (int n = 0; n < 2; ++n) _Pragma("unroll") for (int k = 0; k < 2; ++k) \
;         acc[ai][bj][m][n] = __builtin_amdgcn_mfma_f32_16x16x32_bf16(Bt[n][k], At[m][k], acc[ai][bj][m][n], 0, 0, 0); __builtin_amdgcn_s_setprio(0); } while (0)
; #define PG8_WAIT_V(n) asm volatile("s_waitcnt vmcnt(" #n ")" ::: "memory")
; #define PG8_WAIT_L(n) asm volatile("s_waitcnt lgkmcnt(" #n ")" ::: "memory")
; #define PG8_BAR __builtin_amdgcn_s_barrier()
; #define PG8_SCHED __builtin_amdgcn_sched_barrier(0)
; template <class Epi, class Sched, bool ALIGN_EPI = false, bool SP2 = false>
; __device__ __forceinline__ void gemm_phase(PG8_LAS unsigned char* lds, const Gemm g, const Sched& S, const Epi& E) {
;     ...
;             PG8_LDB(B0, 1, 0); PG8_LDB(B1, 1, 1); PG8_SCHED; PG8_LDA(At, 1, 0); PG8_STAGE(PG8_SA(0, 1), a2 + hstep, voffA);
;             PG8_WAIT_V(8); PG8_WAIT_L(0); PG8_BAR; PG8_MMA(0, 0, At, B0); PG8_MMA(0, 1, At, B1); PG8_BAR; PG8_SCHED;
;             PG8_LDA(At, 1, 1); PG8_STAGE(PG8_SB(1, 0), b3, voffB); PG8_STAGE(PG8_SB(1, 1), b3 + hstep, voffB); PG8_STAGE(PG8_SA(1, 0), a3, voffA);
;             PG8_WAIT_V(8); PG8_WAIT_L(0); PG8_BAR; PG8_MMA(1, 0, At, B0); PG8_MMA(1, 1, At, B1); PG8_BAR; PG8_SCHED;
;     ...
;         if constexpr (ALIGN_EPI) { if (wr == 0) PG8_BAR; }
	s_add_i32 s52, 0, 0x18000
	v_add_u32_e32 v157, s52, v152
	s_add_i32 s53, 0, 0x1c000
	ds_read_b128 v[146:149], v157
	ds_read_b128 v[158:161], v157 offset:1024
	ds_read_b128 v[162:165], v157 offset:2048
	ds_read_b128 v[166:169], v157 offset:3072
	v_add_u32_e32 v157, s53, v152
	ds_read_b128 v[170:173], v157
	ds_read_b128 v[174:177], v157 offset:1024
	ds_read_b128 v[178:181], v157 offset:2048
	ds_read_b128 v[184:187], v157 offset:3072
	s_add_u32 s34, s34, 0x200000
	s_addc_u32 s35, s35, 0
	s_mov_b32 m0, s38
	s_nop 0
	ds_read_b128 v[188:191], v156 offset:32768
	ds_read_b128 v[192:195], v156 offset:33792
	ds_read_b128 v[196:199], v156 offset:34816
	ds_read_b128 v[200:203], v156 offset:35840
	ds_read_b128 v[204:207], v156 offset:36864
	ds_read_b128 v[208:211], v156 offset:37888
	ds_read_b128 v[212:215], v156 offset:38912
	ds_read_b128 v[216:219], v156 offset:39936
	global_load_lds_dwordx4 v130, s[34:35]
	s_nop 0
	s_mov_b32 m0, s39
	s_nop 0
	global_load_lds_dwordx4 v134, s[34:35]
	s_waitcnt vmcnt(8)
	s_waitcnt lgkmcnt(0)
	s_barrier
	s_setprio 1
	s_waitcnt lgkmcnt(0)
	v_mfma_f32_16x16x32_bf16 v[126:129], v[146:149], v[188:191], v[126:129]
	v_mfma_f32_16x16x32_bf16 v[122:125], v[162:165], v[188:191], v[122:125]
	v_mfma_f32_16x16x32_bf16 v[110:113], v[146:149], v[196:199], v[110:113]
	v_mfma_f32_16x16x32_bf16 v[106:109], v[162:165], v[196:199], v[106:109]
	v_mfma_f32_16x16x32_bf16 v[94:97], v[146:149], v[204:207], v[94:97]
	v_mfma_f32_16x16x32_bf16 v[90:93], v[162:165], v[204:207], v[90:93]
	v_mfma_f32_16x16x32_bf16 v[78:81], v[146:149], v[212:215], v[78:81]
	v_mfma_f32_16x16x32_bf16 v[74:77], v[162:165], v[212:215], v[74:77]
	v_mfma_f32_16x16x32_bf16 v[126:129], v[158:161], v[192:195], v[126:129]
	v_mfma_f32_16x16x32_bf16 v[122:125], v[166:169], v[192:195], v[122:125]
	v_mfma_f32_16x16x32_bf16 v[110:113], v[158:161], v[200:203], v[110:113]
	v_mfma_f32_16x16x32_bf16 v[106:109], v[166:169], v[200:203], v[106:109]
	v_mfma_f32_16x16x32_bf16 v[94:97], v[158:161], v[208:211], v[94:97]
	v_mfma_f32_16x16x32_bf16 v[90:93], v[166:169], v[208:211], v[90:93]
	v_mfma_f32_16x16x32_bf16 v[78:81], v[158:161], v[216:219], v[78:81]
	v_mfma_f32_16x16x32_bf16 v[74:77], v[166:169], v[216:219], v[74:77]
	v_mfma_f32_16x16x32_bf16 v[118:121], v[170:173], v[188:191], v[118:121]
	v_mfma_f32_16x16x32_bf16 v[114:117], v[178:181], v[188:191], v[114:117]
	v_mfma_f32_16x16x32_bf16 v[102:105], v[170:173], v[196:199], v[102:105]
	v_mfma_f32_16x16x32_bf16 v[98:101], v[178:181], v[196:199], v[98:101]
	v_mfma_f32_16x16x32_bf16 v[86:89], v[170:173], v[204:207], v[86:89]
	v_mfma_f32_16x16x32_bf16 v[82:85], v[178:181], v[204:207], v[82:85]
	v_mfma_f32_16x16x32_bf16 v[70:73], v[170:173], v[212:215], v[70:73]
	v_mfma_f32_16x16x32_bf16 v[66:69], v[178:181], v[212:215], v[66:69]
	v_mfma_f32_16x16x32_bf16 v[118:121], v[174:177], v[192:195], v[118:121]
	v_mfma_f32_16x16x32_bf16 v[114:117], v[184:187], v[192:195], v[114:117]
	v_mfma_f32_16x16x32_bf16 v[102:105], v[174:177], v[200:203], v[102:105]
	v_mfma_f32_16x16x32_bf16 v[98:101], v[184:187], v[200:203], v[98:101]
	v_mfma_f32_16x16x32_bf16 v[86:89], v[174:177], v[208:211], v[86:89]
	v_mfma_f32_16x16x32_bf16 v[82:85], v[184:187], v[208:211], v[82:85]
	v_mfma_f32_16x16x32_bf16 v[70:73], v[174:177], v[216:219], v[70:73]
	v_mfma_f32_16x16x32_bf16 v[66:69], v[184:187], v[216:219], v[66:69]
	s_setprio 0
	s_barrier
	s_add_i32 s34, s52, s36
	s_add_u32 s58, s30, s2
	s_addc_u32 s59, s31, s3
	s_mov_b32 m0, s34
	ds_read_b128 v[188:191], v156 offset:49152
	ds_read_b128 v[192:195], v156 offset:50176
	ds_read_b128 v[196:199], v156 offset:51200
	ds_read_b128 v[200:203], v156 offset:52224
	ds_read_b128 v[204:207], v156 offset:53248
	ds_read_b128 v[208:211], v156 offset:54272
	ds_read_b128 v[212:215], v156 offset:55296
	ds_read_b128 v[216:219], v156 offset:56320
	global_load_lds_dwordx4 v132, s[58:59]
	s_add_i32 m0, s34, 0x2000
	s_add_u32 s30, s30, 0x200080
	s_nop 0
	s_addc_u32 s31, s31, 0
	s_add_i32 s34, s53, s36
	global_load_lds_dwordx4 v136, s[58:59]
	s_nop 0
	s_mov_b32 m0, s34
	s_nop 0
	global_load_lds_dwordx4 v132, s[30:31]
	s_nop 0
	s_add_i32 m0, s34, 0x2000
	s_nop 0
	global_load_lds_dwordx4 v136, s[30:31]
	s_nop 0
	s_mov_b32 m0, s41
	s_nop 0
	global_load_lds_dwordx4 v130, s[60:61]
	s_nop 0
	s_mov_b32 m0, s42
	s_nop 0
	global_load_lds_dwordx4 v134, s[60:61]
	s_waitcnt vmcnt(8)
	s_waitcnt lgkmcnt(0)
	s_barrier
	s_setprio 1
	s_waitcnt lgkmcnt(0)
	v_mfma_f32_16x16x32_bf16 v[62:65], v[146:149], v[188:191], v[62:65]
	v_mfma_f32_16x16x32_bf16 v[58:61], v[162:165], v[188:191], v[58:61]
	v_mfma_f32_16x16x32_bf16 v[46:49], v[146:149], v[196:199], v[46:49]
	v_mfma_f32_16x16x32_bf16 v[42:45], v[162:165], v[196:199], v[42:45]
	v_mfma_f32_16x16x32_bf16 v[30:33], v[146:149], v[204:207], v[30:33]
	v_mfma_f32_16x16x32_bf16 v[26:29], v[162:165], v[204:207], v[26:29]
	v_mfma_f32_16x16x32_bf16 v[14:17], v[146:149], v[212:215], v[14:17]
	v_mfma_f32_16x16x32_bf16 v[10:13], v[162:165], v[212:215], v[10:13]
	v_mfma_f32_16x16x32_bf16 v[62:65], v[158:161], v[192:195], v[62:65]
	v_mfma_f32_16x16x32_bf16 v[58:61], v[166:169], v[192:195], v[58:61]
	v_mfma_f32_16x16x32_bf16 v[46:49], v[158:161], v[200:203], v[46:49]
	v_mfma_f32_16x16x32_bf16 v[42:45], v[166:169], v[200:203], v[42:45]
	v_mfma_f32_16x16x32_bf16 v[30:33], v[158:161], v[208:211], v[30:33]
	v_mfma_f32_16x16x32_bf16 v[26:29], v[166:169], v[208:211], v[26:29]
	v_mfma_f32_16x16x32_bf16 v[14:17], v[158:161], v[216:219], v[14:17]
	v_mfma_f32_16x16x32_bf16 v[10:13], v[166:169], v[216:219], v[10:13]
	v_mfma_f32_16x16x32_bf16 v[54:57], v[170:173], v[188:191], v[54:57]
	v_mfma_f32_16x16x32_bf16 v[50:53], v[178:181], v[188:191], v[50:53]
	v_mfma_f32_16x16x32_bf16 v[38:41], v[170:173], v[196:199], v[38:41]
	v_mfma_f32_16x16x32_bf16 v[34:37], v[178:181], v[196:199], v[34:37]
	v_mfma_f32_16x16x32_bf16 v[22:25], v[170:173], v[204:207], v[22:25]
	v_mfma_f32_16x16x32_bf16 v[18:21], v[178:181], v[204:207], v[18:21]
	v_mfma_f32_16x16x32_bf16 v[6:9], v[170:173], v[212:215], v[6:9]
	v_mfma_f32_16x16x32_bf16 v[2:5], v[178:181], v[212:215], v[2:5]
	v_mfma_f32_16x16x32_bf16 v[54:57], v[174:177], v[192:195], v[54:57]
	v_mfma_f32_16x16x32_bf16 v[50:53], v[184:187], v[192:195], v[50:53]
	v_mfma_f32_16x16x32_bf16 v[38:41], v[174:177], v[200:203], v[38:41]
	v_mfma_f32_16x16x32_bf16 v[34:37], v[184:187], v[200:203], v[34:37]
	v_mfma_f32_16x16x32_bf16 v[22:25], v[174:177], v[208:211], v[22:25]
	v_mfma_f32_16x16x32_bf16 v[18:21], v[184:187], v[208:211], v[18:21]
	v_mfma_f32_16x16x32_bf16 v[6:9], v[174:177], v[216:219], v[6:9]
	v_mfma_f32_16x16x32_bf16 v[2:5], v[184:187], v[216:219], v[2:5]
	s_setprio 0
	s_barrier
	s_add_i32 s51, s51, 2
	s_add_u32 s28, s28, 0x100
	s_addc_u32 s29, s29, 0
	s_add_u32 s49, s49, 0x100
	s_addc_u32 s50, s50, 0
	s_cmpk_gt_u32 s51, 0x7d
	s_cbranch_scc0 .LBB0_563
	s_and_b64 vcc, exec, s[8:9]
	s_cbranch_vccz .LBB0_566
	s_barrier

; #define PG8_STAGE(bufoff, gbase, voff) do { _Pragma("unroll") for (int _i = 0; _i < 2; ++_i) \
;         __builtin_amdgcn_global_load_lds((const unsigned*)((const char*)(gbase) + (voff)[_i]), (PG8_LAS unsigned*)(lds + (bufoff) + ldsw + _i * 8192), 16, 0, 0); } while (0)
; #define PG8_LDA(dst, b, h) do { _Pragma("unroll") for (int m = 0; m < 4; ++m) _Pragma("unroll") for (int k = 0; k < 2; ++k) dst[m][k] = *(const PG8_LAS bf16x8*)(lds + PG8_SA(b, h) + aoff + m * 2048 + k * 1024); } while (0)
; #define PG8_LDB(dst, b, h) do { _Pragma("unroll") for (int n = 0; n < 2; ++n) _Pragma("unroll") for (int k = 0; k < 2; ++k) dst[n][k] = *(const PG8_LAS bf16x8*)(lds + PG8_SB(b, h) + boff + n * 2048 + k * 1024); } while (0)
; #define PG8_WAIT_V(n) asm volatile("s_waitcnt vmcnt(" #n ")" ::: "memory")
; #define PG8_WAIT_L(n) asm volatile("s_waitcnt lgkmcnt(" #n ")" ::: "memory")
; #define PG8_BAR __builtin_amdgcn_s_barrier()
; template <class Epi, class Sched, bool ALIGN_EPI = false, bool SP2 = false>
; __device__ __forceinline__ void gemm_phase(PG8_LAS unsigned char* lds, const Gemm g, const Sched& S, const Epi& E) {
;     ...
;         const bool has_next = S.next(ui + 1, nxt);
;         const char* nA = has_next ? (const char*)g.A + (size_t)nxt.pm * tstep : cA; const char* nB = has_next ? (const char*)g.Bt + (size_t)nxt.pn * tstep : cB;
;         for (int t = 0; t < nt; t += 2) {
;             const bool last = (t == nt - 2);
;             const char* a1 = cA + (size_t)(t + 1) * kstep;
;             const char* a2 = last ? nA : cA + (size_t)(t + 2) * kstep; const char* b2 = last ? nB : cB + (size_t)(t + 2) * kstep;
;             const char* a3 = a2 + kstep; const char* b3 = b2 + kstep;
;             if (last && has_next) S.a_ready(nxt);
;             if constexpr (SP2) {
;             PG8_LDB(B0, 0, 0); PG8_LDB(B1, 0, 1); PG8_SCHED; PG8_LDA(At, 0, 0); PG8_STAGE(PG8_SA(1, 1), a1 + hstep, voffA);
;             PG8_WAIT_V(8); PG8_WAIT_L(0); PG8_BAR; PG8_MMA(0, 0, At, B0); PG8_MMA(0, 1, At, B1); PG8_BAR; PG8_SCHED;
;     ...
; #pragma unroll
;         for (int a = 0; a < 2; ++a)
; #pragma unroll
;             for (int b = 0; b < 2; ++b)
; #pragma unroll
;                 for (int m = 0; m < 4; ++m)
; #pragma unroll
;                     for (int n = 0; n < 2; ++n) acc[a][b][m][n] = (f32x4){0.f, 0.f, 0.f, 0.f};
;         cur = nxt; cA = nA; cB = nB; ++ui;
.LBB0_706:
	s_ashr_i32 s25, s24, 31
	s_lshl_b64 s[26:27], s[24:25], 21
	s_add_u32 s26, s6, s26
	s_addc_u32 s27, s7, s27
	s_and_b64 s[28:29], s[4:5], exec
	s_cselect_b32 s25, s27, s31
	s_cselect_b32 s57, s26, s30
	s_ashr_i32 s23, s22, 31
	s_lshl_b64 s[28:29], s[22:23], 21
	v_readlane_b32 s23, v249, 30
	s_add_u32 s28, s23, s28
	v_readlane_b32 s23, v249, 31
	s_addc_u32 s29, s23, s29
	s_and_b64 s[36:37], s[4:5], exec
	s_cselect_b32 s23, s29, s35
	s_cselect_b32 s58, s28, s34
	s_add_u32 s30, s30, 0x100080
	s_addc_u32 s31, s31, 0
	s_add_u32 s59, s34, 0x100
	v_mov_b32_e32 v2, 0
	s_addc_u32 s60, s35, 0
	s_mov_b32 s61, -2
	v_mov_b32_e32 v3, v2
	v_mov_b32_e32 v4, v2
	v_mov_b32_e32 v5, v2
	v_mov_b32_e32 v6, v2
	v_mov_b32_e32 v7, v2
	v_mov_b32_e32 v8, v2
	v_mov_b32_e32 v9, v2
	v_mov_b32_e32 v18, v2
	v_mov_b32_e32 v19, v2
	v_mov_b32_e32 v20, v2
	v_mov_b32_e32 v21, v2
	v_mov_b32_e32 v22, v2
	v_mov_b32_e32 v23, v2
	v_mov_b32_e32 v24, v2
	v_mov_b32_e32 v25, v2
	v_mov_b32_e32 v30, v2
	v_mov_b32_e32 v31, v2
	v_mov_b32_e32 v32, v2
	v_mov_b32_e32 v33, v2
	v_mov_b32_e32 v38, v2
	v_mov_b32_e32 v39, v2
	v_mov_b32_e32 v40, v2
	v_mov_b32_e32 v41, v2
	v_mov_b32_e32 v46, v2
	v_mov_b32_e32 v47, v2
	v_mov_b32_e32 v48, v2
	v_mov_b32_e32 v49, v2
	v_mov_b32_e32 v54, v2
	v_mov_b32_e32 v55, v2
	v_mov_b32_e32 v56, v2
	v_mov_b32_e32 v57, v2
	v_mov_b32_e32 v10, v2
	v_mov_b32_e32 v11, v2
	v_mov_b32_e32 v12, v2
	v_mov_b32_e32 v13, v2
	v_mov_b32_e32 v14, v2
	v_mov_b32_e32 v15, v2
	v_mov_b32_e32 v16, v2
	v_mov_b32_e32 v17, v2
	v_mov_b32_e32 v26, v2
	v_mov_b32_e32 v27, v2
	v_mov_b32_e32 v28, v2
	v_mov_b32_e32 v29, v2
	v_mov_b32_e32 v34, v2
	v_mov_b32_e32 v35, v2
	v_mov_b32_e32 v36, v2
	v_mov_b32_e32 v37, v2
	v_mov_b32_e32 v42, v2
	v_mov_b32_e32 v43, v2
	v_mov_b32_e32 v44, v2
	v_mov_b32_e32 v45, v2
	v_mov_b32_e32 v50, v2
	v_mov_b32_e32 v51, v2
	v_mov_b32_e32 v52, v2
	v_mov_b32_e32 v53, v2
	v_mov_b32_e32 v58, v2
	v_mov_b32_e32 v59, v2
	v_mov_b32_e32 v60, v2
	v_mov_b32_e32 v61, v2
	v_mov_b32_e32 v62, v2
	v_mov_b32_e32 v63, v2
	v_mov_b32_e32 v64, v2
	v_mov_b32_e32 v65, v2
	s_waitcnt vmcnt(0)
	v_mov_b32_e32 v66, v2
	v_mov_b32_e32 v67, v2
	v_mov_b32_e32 v68, v2
	v_mov_b32_e32 v69, v2
	v_mov_b32_e32 v70, v2
	v_mov_b32_e32 v71, v2
	v_mov_b32_e32 v72, v2
	v_mov_b32_e32 v73, v2
	v_mov_b32_e32 v74, v2
	v_mov_b32_e32 v75, v2
	v_mov_b32_e32 v76, v2
	v_mov_b32_e32 v77, v2
	v_mov_b32_e32 v82, v2
	v_mov_b32_e32 v83, v2
	v_mov_b32_e32 v84, v2
	v_mov_b32_e32 v85, v2
	v_mov_b32_e32 v98, v2
	v_mov_b32_e32 v99, v2
	v_mov_b32_e32 v100, v2
	v_mov_b32_e32 v101, v2
	v_mov_b32_e32 v102, v2
	v_mov_b32_e32 v103, v2
	v_mov_b32_e32 v104, v2
	v_mov_b32_e32 v105, v2
	v_mov_b32_e32 v114, v2
	v_mov_b32_e32 v115, v2
	v_mov_b32_e32 v116, v2
	v_mov_b32_e32 v117, v2
	v_mov_b32_e32 v118, v2
	v_mov_b32_e32 v119, v2
	v_mov_b32_e32 v120, v2
	v_mov_b32_e32 v121, v2
	v_mov_b32_e32 v78, v2
	v_mov_b32_e32 v79, v2
	v_mov_b32_e32 v80, v2
	v_mov_b32_e32 v81, v2
	v_mov_b32_e32 v86, v2
	v_mov_b32_e32 v87, v2
	v_mov_b32_e32 v88, v2
	v_mov_b32_e32 v89, v2
	v_mov_b32_e32 v90, v2
	v_mov_b32_e32 v91, v2
	v_mov_b32_e32 v92, v2
	v_mov_b32_e32 v93, v2
	v_mov_b32_e32 v94, v2
	v_mov_b32_e32 v95, v2
	v_mov_b32_e32 v96, v2
	v_mov_b32_e32 v97, v2
	v_mov_b32_e32 v106, v2
	v_mov_b32_e32 v107, v2
	v_mov_b32_e32 v108, v2
	v_mov_b32_e32 v109, v2
	v_mov_b32_e32 v110, v2
	v_mov_b32_e32 v111, v2
	v_mov_b32_e32 v112, v2
	v_mov_b32_e32 v113, v2
	v_mov_b32_e32 v122, v2
	v_mov_b32_e32 v123, v2
	v_mov_b32_e32 v124, v2
	v_mov_b32_e32 v125, v2
	v_mov_b32_e32 v126, v2
	v_mov_b32_e32 v127, v2
	v_mov_b32_e32 v128, v2
	v_mov_b32_e32 v129, v2
	s_nop 0
	s_nop 0
	s_nop 0
	s_nop 0
	s_nop 0
	s_nop 0
	s_nop 0
	s_nop 0
	s_nop 0
	s_nop 0
	s_nop 0
	s_nop 0
	s_nop 0
	s_nop 0
.LBB0_707:
	ds_read_b128 v[142:145], v151
	ds_read_b128 v[154:157], v151 offset:1024
	ds_read_b128 v[158:161], v151 offset:2048
	ds_read_b128 v[162:165], v151 offset:3072
	ds_read_b128 v[166:169], v152
	ds_read_b128 v[170:173], v152 offset:1024
	ds_read_b128 v[174:177], v152 offset:2048
	ds_read_b128 v[178:181], v152 offset:3072
	s_add_u32 s34, s30, 0xfff00080
	s_addc_u32 s35, s31, -1
	s_cmp_eq_u32 s61, 60
	s_cselect_b32 s37, s25, s35
	s_cselect_b32 s36, s57, s34
	s_cselect_b32 s35, s23, s60
	s_cselect_b32 s34, s58, s59
	s_nop 0
	s_add_i32 m0, s42, 0xc000
	ds_read_b128 v[184:187], v153
	ds_read_b128 v[188:191], v153 offset:1024
	ds_read_b128 v[192:195], v153 offset:2048
	ds_read_b128 v[196:199], v153 offset:3072
	ds_read_b128 v[200:203], v153 offset:4096
	ds_read_b128 v[204:207], v153 offset:5120
	ds_read_b128 v[208:211], v153 offset:6144
	ds_read_b128 v[212:215], v153 offset:7168
	global_load_lds_dwordx4 v134, s[30:31]
	s_nop 0
	s_add_i32 m0, s42, 0xe000
	s_nop 0
	global_load_lds_dwordx4 v136, s[30:31]
	s_waitcnt vmcnt(8)
	s_waitcnt lgkmcnt(0)
	s_barrier
; #define PG8_STAGE(bufoff, gbase, voff) do { _Pragma("unroll") for (int _i = 0; _i < 2; ++_i) \
;         __builtin_amdgcn_global_load_lds((const unsigned*)((const char*)(gbase) + (voff)[_i]), (PG8_LAS unsigned*)(lds + (bufoff) + ldsw + _i * 8192), 16, 0, 0); } while (0)
; #define PG8_LDA(dst, b, h) do { _Pragma("unroll") for (int m = 0; m < 4; ++m) _Pragma("unroll") for (int k = 0; k < 2; ++k) dst[m][k] = *(const PG8_LAS bf16x8*)(lds + PG8_SA(b, h) + aoff + m * 2048 + k * 1024); } while (0)
; #define PG8_MMA(ai, bj, At, Bt) do { __builtin_amdgcn_s_setprio(1); _Pragma("unroll") for (int m = 0; m < 4; ++m) _Pragma("unroll") for (int n = 0; n < 2; ++n) _Pragma("unroll") for (int k = 0; k < 2; ++k) \
;         acc[ai][bj][m][n] = __builtin_amdgcn_mfma_f32_16x16x32_bf16(Bt[n][k], At[m][k], acc[ai][bj][m][n], 0, 0, 0); __builtin_amdgcn_s_setprio(0); } while (0)
; #define PG8_WAIT_V(n) asm volatile("s_waitcnt vmcnt(" #n ")" ::: "memory")
; #define PG8_WAIT_L(n) asm volatile("s_waitcnt lgkmcnt(" #n ")" ::: "memory")
; #define PG8_BAR __builtin_amdgcn_s_barrier()
; #define PG8_SCHED __builtin_amdgcn_sched_barrier(0)
; template <class Epi, class Sched, bool ALIGN_EPI = false, bool SP2 = false>
; __device__ __forceinline__ void gemm_phase(PG8_LAS unsigned char* lds, const Gemm g, const Sched& S, const Epi& E) {
;     ...
;             PG8_WAIT_V(8); PG8_WAIT_L(0); PG8_BAR; PG8_MMA(0, 0, At, B0); PG8_MMA(0, 1, At, B1); PG8_BAR; PG8_SCHED;
;             PG8_LDA(At, 0, 1); PG8_STAGE(PG8_SB(0, 0), b2, voffB); PG8_STAGE(PG8_SB(0, 1), b2 + hstep, voffB); PG8_STAGE(PG8_SA(0, 0), a2, voffA);
;             PG8_WAIT_V(8); PG8_WAIT_L(0); PG8_BAR; PG8_MMA(1, 0, At, B0); PG8_MMA(1, 1, At, B1); PG8_BAR; PG8_SCHED;
	s_setprio 1
	s_waitcnt lgkmcnt(0)
	v_mfma_f32_16x16x32_bf16 v[126:129], v[142:145], v[184:187], v[126:129]
	v_mfma_f32_16x16x32_bf16 v[122:125], v[158:161], v[184:187], v[122:125]
	v_mfma_f32_16x16x32_bf16 v[110:113], v[142:145], v[192:195], v[110:113]
	v_mfma_f32_16x16x32_bf16 v[106:109], v[158:161], v[192:195], v[106:109]
	v_mfma_f32_16x16x32_bf16 v[94:97], v[142:145], v[200:203], v[94:97]
	v_mfma_f32_16x16x32_bf16 v[90:93], v[158:161], v[200:203], v[90:93]
	v_mfma_f32_16x16x32_bf16 v[86:89], v[142:145], v[208:211], v[86:89]
	v_mfma_f32_16x16x32_bf16 v[78:81], v[158:161], v[208:211], v[78:81]
	v_mfma_f32_16x16x32_bf16 v[126:129], v[154:157], v[188:191], v[126:129]
	v_mfma_f32_16x16x32_bf16 v[122:125], v[162:165], v[188:191], v[122:125]
	v_mfma_f32_16x16x32_bf16 v[110:113], v[154:157], v[196:199], v[110:113]
	v_mfma_f32_16x16x32_bf16 v[106:109], v[162:165], v[196:199], v[106:109]
	v_mfma_f32_16x16x32_bf16 v[94:97], v[154:157], v[204:207], v[94:97]
	v_mfma_f32_16x16x32_bf16 v[90:93], v[162:165], v[204:207], v[90:93]
	v_mfma_f32_16x16x32_bf16 v[86:89], v[154:157], v[212:215], v[86:89]
	v_mfma_f32_16x16x32_bf16 v[78:81], v[162:165], v[212:215], v[78:81]
	v_mfma_f32_16x16x32_bf16 v[118:121], v[166:169], v[184:187], v[118:121]
	v_mfma_f32_16x16x32_bf16 v[114:117], v[174:177], v[184:187], v[114:117]
	v_mfma_f32_16x16x32_bf16 v[102:105], v[166:169], v[192:195], v[102:105]
	v_mfma_f32_16x16x32_bf16 v[98:101], v[174:177], v[192:195], v[98:101]
	v_mfma_f32_16x16x32_bf16 v[82:85], v[166:169], v[200:203], v[82:85]
	v_mfma_f32_16x16x32_bf16 v[74:77], v[174:177], v[200:203], v[74:77]
	v_mfma_f32_16x16x32_bf16 v[70:73], v[166:169], v[208:211], v[70:73]
	v_mfma_f32_16x16x32_bf16 v[66:69], v[174:177], v[208:211], v[66:69]
	v_mfma_f32_16x16x32_bf16 v[118:121], v[170:173], v[188:191], v[118:121]
	v_mfma_f32_16x16x32_bf16 v[114:117], v[178:181], v[188:191], v[114:117]
	v_mfma_f32_16x16x32_bf16 v[102:105], v[170:173], v[196:199], v[102:105]
	v_mfma_f32_16x16x32_bf16 v[98:101], v[178:181], v[196:199], v[98:101]
	v_mfma_f32_16x16x32_bf16 v[82:85], v[170:173], v[204:207], v[82:85]
	v_mfma_f32_16x16x32_bf16 v[74:77], v[178:181], v[204:207], v[74:77]
	v_mfma_f32_16x16x32_bf16 v[70:73], v[170:173], v[212:215], v[70:73]
	v_mfma_f32_16x16x32_bf16 v[66:69], v[178:181], v[212:215], v[66:69]
	s_setprio 0
	s_barrier
	s_add_i32 s62, s51, s33
	s_nop 0
	s_mov_b32 m0, s62
	ds_read_b128 v[184:187], v153 offset:16384
	ds_read_b128 v[188:191], v153 offset:17408
	ds_read_b128 v[192:195], v153 offset:18432
	ds_read_b128 v[196:199], v153 offset:19456
	ds_read_b128 v[200:203], v153 offset:20480
	ds_read_b128 v[204:207], v153 offset:21504
	ds_read_b128 v[208:211], v153 offset:22528
	ds_read_b128 v[212:215], v153 offset:23552
	global_load_lds_dwordx4 v130, s[34:35]
	s_add_i32 m0, s62, 0x2000
	s_add_u32 s62, s34, 0x100000
	s_nop 0
	s_addc_u32 s63, s35, 0
	s_add_i32 s72, s52, s33
	global_load_lds_dwordx4 v132, s[34:35]
	s_nop 0
	s_mov_b32 m0, s72
	s_add_u32 s84, s36, s12
	s_addc_u32 s85, s37, s13
	global_load_lds_dwordx4 v130, s[62:63]
	s_nop 0
	s_add_i32 m0, s72, 0x2000
	s_nop 0
	global_load_lds_dwordx4 v132, s[62:63]
	s_nop 0
	s_mov_b32 m0, s42
	s_nop 0
	global_load_lds_dwordx4 v130, s[36:37]
	s_mov_b32 m0, s43
	s_nop 0
	global_load_lds_dwordx4 v132, s[36:37]
	s_waitcnt vmcnt(8)
	s_waitcnt lgkmcnt(0)
	s_barrier
	s_setprio 1
	s_waitcnt lgkmcnt(0)
	v_mfma_f32_16x16x32_bf16 v[62:65], v[142:145], v[184:187], v[62:65]
	v_mfma_f32_16x16x32_bf16 v[58:61], v[158:161], v[184:187], v[58:61]
	v_mfma_f32_16x16x32_bf16 v[50:53], v[142:145], v[192:195], v[50:53]
	v_mfma_f32_16x16x32_bf16 v[42:45], v[158:161], v[192:195], v[42:45]
	v_mfma_f32_16x16x32_bf16 v[34:37], v[142:145], v[200:203], v[34:37]
	v_mfma_f32_16x16x32_bf16 v[26:29], v[158:161], v[200:203], v[26:29]
	v_mfma_f32_16x16x32_bf16 v[14:17], v[142:145], v[208:211], v[14:17]
	v_mfma_f32_16x16x32_bf16 v[10:13], v[158:161], v[208:211], v[10:13]
	v_mfma_f32_16x16x32_bf16 v[62:65], v[154:157], v[188:191], v[62:65]
	v_mfma_f32_16x16x32_bf16 v[58:61], v[162:165], v[188:191], v[58:61]
	v_mfma_f32_16x16x32_bf16 v[50:53], v[154:157], v[196:199], v[50:53]
	v_mfma_f32_16x16x32_bf16 v[42:45], v[162:165], v[196:199], v[42:45]
	v_mfma_f32_16x16x32_bf16 v[34:37], v[154:157], v[204:207], v[34:37]
	v_mfma_f32_16x16x32_bf16 v[26:29], v[162:165], v[204:207], v[26:29]
	v_mfma_f32_16x16x32_bf16 v[14:17], v[154:157], v[212:215], v[14:17]
	v_mfma_f32_16x16x32_bf16 v[10:13], v[162:165], v[212:215], v[10:13]
	v_mfma_f32_16x16x32_bf16 v[54:57], v[166:169], v[184:187], v[54:57]
	v_mfma_f32_16x16x32_bf16 v[46:49], v[174:177], v[184:187], v[46:49]
	v_mfma_f32_16x16x32_bf16 v[38:41], v[166:169], v[192:195], v[38:41]
	v_mfma_f32_16x16x32_bf16 v[30:33], v[174:177], v[192:195], v[30:33]
	v_mfma_f32_16x16x32_bf16 v[22:25], v[166:169], v[200:203], v[22:25]
	v_mfma_f32_16x16x32_bf16 v[18:21], v[174:177], v[200:203], v[18:21]
	v_mfma_f32_16x16x32_bf16 v[6:9], v[166:169], v[208:211], v[6:9]
	v_mfma_f32_16x16x32_bf16 v[2:5], v[174:177], v[208:211], v[2:5]
	v_mfma_f32_16x16x32_bf16 v[54:57], v[170:173], v[188:191], v[54:57]
	v_mfma_f32_16x16x32_bf16 v[46:49], v[178:181], v[188:191], v[46:49]
	v_mfma_f32_16x16x32_bf16 v[38:41], v[170:173], v[196:199], v[38:41]
	v_mfma_f32_16x16x32_bf16 v[30:33], v[178:181], v[196:199], v[30:33]
	v_mfma_f32_16x16x32_bf16 v[22:25], v[170:173], v[204:207], v[22:25]
	v_mfma_f32_16x16x32_bf16 v[18:21], v[178:181], v[204:207], v[18:21]
	v_mfma_f32_16x16x32_bf16 v[6:9], v[170:173], v[212:215], v[6:9]
	v_mfma_f32_16x16x32_bf16 v[2:5], v[178:181], v[212:215], v[2:5]
	s_setprio 0
	s_barrier
; #define PG8_STAGE(bufoff, gbase, voff) do { _Pragma("unroll") for (int _i = 0; _i < 2; ++_i) \
;         __builtin_amdgcn_global_load_lds((const unsigned*)((const char*)(gbase) + (voff)[_i]), (PG8_LAS unsigned*)(lds + (bufoff) + ldsw + _i * 8192), 16, 0, 0); } while (0)
; #define PG8_LDA(dst, b, h) do { _Pragma("unroll") for (int m = 0; m < 4; ++m) _Pragma("unroll") for (int k = 0; k < 2; ++k) dst[m][k] = *(const PG8_LAS bf16x8*)(lds + PG8_SA(b, h) + aoff + m * 2048 + k * 1024); } while (0)
; #define PG8_LDB(dst, b, h) do { _Pragma("unroll") for (int n = 0; n < 2; ++n) _Pragma("unroll") for (int k = 0; k < 2; ++k) dst[n][k] = *(const PG8_LAS bf16x8*)(lds + PG8_SB(b, h) + boff + n * 2048 + k * 1024); } while (0)
; #define PG8_MMA(ai, bj, At, Bt) do { __builtin_amdgcn_s_setprio(1); _Pragma("unroll") for (int m = 0; m < 4; ++m) _Pragma("unroll") for (int n = 0; n < 2; ++n) _Pragma("unroll") for (int k = 0; k < 2; ++k) \
;         acc[ai][bj][m][n] = __builtin_amdgcn_mfma_f32_16x16x32_bf16(Bt[n][k], At[m][k], acc[ai][bj][m][n], 0, 0, 0); __builtin_amdgcn_s_setprio(0); } while (0)
; #define PG8_WAIT_V(n) asm volatile("s_waitcnt vmcnt(" #n ")" ::: "memory")
; #define PG8_WAIT_L(n) asm volatile("s_waitcnt lgkmcnt(" #n ")" ::: "memory")
; #define PG8_BAR __builtin_amdgcn_s_barrier()
; #define PG8_SCHED __builtin_amdgcn_sched_barrier(0)
; template <class Epi, class Sched, bool ALIGN_EPI = false, bool SP2 = false>
; __device__ __forceinline__ void gemm_phase(PG8_LAS unsigned char* lds, const Gemm g, const Sched& S, const Epi& E) {
;     ...
;             PG8_LDB(B0, 1, 0); PG8_LDB(B1, 1, 1); PG8_SCHED; PG8_LDA(At, 1, 0); PG8_STAGE(PG8_SA(0, 1), a2 + hstep, voffA);
;             PG8_WAIT_V(8); PG8_WAIT_L(0); PG8_BAR; PG8_MMA(0, 0, At, B0); PG8_MMA(0, 1, At, B1); PG8_BAR; PG8_SCHED;
;             PG8_LDA(At, 1, 1); PG8_STAGE(PG8_SB(1, 0), b3, voffB); PG8_STAGE(PG8_SB(1, 1), b3 + hstep, voffB); PG8_STAGE(PG8_SA(1, 0), a3, voffA);
;             PG8_WAIT_V(8); PG8_WAIT_L(0); PG8_BAR; PG8_MMA(1, 0, At, B0); PG8_MMA(1, 1, At, B1); PG8_BAR; PG8_SCHED;
;     ...
;         if constexpr (ALIGN_EPI) { if (wr == 0) PG8_BAR; }
	s_add_i32 s62, 0, 0x18000
	s_add_i32 s63, 0, 0x1c000
	v_add_u32_e32 v162, s62, v149
	v_add_u32_e32 v178, s63, v149
	ds_read_b128 v[142:145], v162
	ds_read_b128 v[154:157], v162 offset:1024
	ds_read_b128 v[158:161], v162 offset:2048
	ds_read_b128 v[162:165], v162 offset:3072
	ds_read_b128 v[166:169], v178
	ds_read_b128 v[170:173], v178 offset:1024
	ds_read_b128 v[174:177], v178 offset:2048
	ds_read_b128 v[178:181], v178 offset:3072
	s_add_u32 s36, s36, 0x100000
	s_addc_u32 s37, s37, 0
	s_mov_b32 m0, s44
	s_nop 0
	ds_read_b128 v[184:187], v153 offset:32768
	ds_read_b128 v[188:191], v153 offset:33792
	ds_read_b128 v[192:195], v153 offset:34816
	ds_read_b128 v[196:199], v153 offset:35840
	ds_read_b128 v[200:203], v153 offset:36864
	ds_read_b128 v[204:207], v153 offset:37888
	ds_read_b128 v[208:211], v153 offset:38912
	ds_read_b128 v[212:215], v153 offset:39936
	global_load_lds_dwordx4 v130, s[36:37]
	s_nop 0
	s_mov_b32 m0, s45
	s_nop 0
	global_load_lds_dwordx4 v132, s[36:37]
	s_waitcnt vmcnt(8)
	s_waitcnt lgkmcnt(0)
	s_barrier
	s_setprio 1
	s_waitcnt lgkmcnt(0)
	v_mfma_f32_16x16x32_bf16 v[126:129], v[142:145], v[184:187], v[126:129]
	v_mfma_f32_16x16x32_bf16 v[122:125], v[158:161], v[184:187], v[122:125]
	v_mfma_f32_16x16x32_bf16 v[110:113], v[142:145], v[192:195], v[110:113]
	v_mfma_f32_16x16x32_bf16 v[106:109], v[158:161], v[192:195], v[106:109]
	v_mfma_f32_16x16x32_bf16 v[94:97], v[142:145], v[200:203], v[94:97]
	v_mfma_f32_16x16x32_bf16 v[90:93], v[158:161], v[200:203], v[90:93]
	v_mfma_f32_16x16x32_bf16 v[86:89], v[142:145], v[208:211], v[86:89]
	v_mfma_f32_16x16x32_bf16 v[78:81], v[158:161], v[208:211], v[78:81]
	v_mfma_f32_16x16x32_bf16 v[126:129], v[154:157], v[188:191], v[126:129]
	v_mfma_f32_16x16x32_bf16 v[122:125], v[162:165], v[188:191], v[122:125]
	v_mfma_f32_16x16x32_bf16 v[110:113], v[154:157], v[196:199], v[110:113]
	v_mfma_f32_16x16x32_bf16 v[106:109], v[162:165], v[196:199], v[106:109]
	v_mfma_f32_16x16x32_bf16 v[94:97], v[154:157], v[204:207], v[94:97]
	v_mfma_f32_16x16x32_bf16 v[90:93], v[162:165], v[204:207], v[90:93]
	v_mfma_f32_16x16x32_bf16 v[86:89], v[154:157], v[212:215], v[86:89]
	v_mfma_f32_16x16x32_bf16 v[78:81], v[162:165], v[212:215], v[78:81]
	v_mfma_f32_16x16x32_bf16 v[118:121], v[166:169], v[184:187], v[118:121]
	v_mfma_f32_16x16x32_bf16 v[114:117], v[174:177], v[184:187], v[114:117]
	v_mfma_f32_16x16x32_bf16 v[102:105], v[166:169], v[192:195], v[102:105]
	v_mfma_f32_16x16x32_bf16 v[98:101], v[174:177], v[192:195], v[98:101]
	v_mfma_f32_16x16x32_bf16 v[82:85], v[166:169], v[200:203], v[82:85]
	v_mfma_f32_16x16x32_bf16 v[74:77], v[174:177], v[200:203], v[74:77]
	v_mfma_f32_16x16x32_bf16 v[70:73], v[166:169], v[208:211], v[70:73]
	v_mfma_f32_16x16x32_bf16 v[66:69], v[174:177], v[208:211], v[66:69]
	v_mfma_f32_16x16x32_bf16 v[118:121], v[170:173], v[188:191], v[118:121]
	v_mfma_f32_16x16x32_bf16 v[114:117], v[178:181], v[188:191], v[114:117]
	v_mfma_f32_16x16x32_bf16 v[102:105], v[170:173], v[196:199], v[102:105]
	v_mfma_f32_16x16x32_bf16 v[98:101], v[178:181], v[196:199], v[98:101]
	v_mfma_f32_16x16x32_bf16 v[82:85], v[170:173], v[204:207], v[82:85]
	v_mfma_f32_16x16x32_bf16 v[74:77], v[178:181], v[204:207], v[74:77]
	v_mfma_f32_16x16x32_bf16 v[70:73], v[170:173], v[212:215], v[70:73]
	v_mfma_f32_16x16x32_bf16 v[66:69], v[178:181], v[212:215], v[66:69]
	s_setprio 0
	s_barrier
	s_add_i32 s36, s62, s33
	s_add_u32 s82, s34, s12
	s_addc_u32 s83, s35, s13
	s_mov_b32 m0, s36
	ds_read_b128 v[184:187], v153 offset:49152
	ds_read_b128 v[188:191], v153 offset:50176
	ds_read_b128 v[192:195], v153 offset:51200
	ds_read_b128 v[196:199], v153 offset:52224
	ds_read_b128 v[200:203], v153 offset:53248
	ds_read_b128 v[204:207], v153 offset:54272
	ds_read_b128 v[208:211], v153 offset:55296
	ds_read_b128 v[212:215], v153 offset:56320
	global_load_lds_dwordx4 v130, s[82:83]
	s_add_i32 m0, s36, 0x2000
	s_add_u32 s34, s34, 0x100080
	s_nop 0
	s_addc_u32 s35, s35, 0
	s_add_i32 s36, s63, s33
	global_load_lds_dwordx4 v132, s[82:83]
	s_nop 0
	s_mov_b32 m0, s36
	s_nop 0
	global_load_lds_dwordx4 v130, s[34:35]
	s_nop 0
	s_add_i32 m0, s36, 0x2000
	s_nop 0
	global_load_lds_dwordx4 v132, s[34:35]
	s_nop 0
	s_mov_b32 m0, s49
	s_nop 0
	global_load_lds_dwordx4 v130, s[84:85]
	s_nop 0
	s_mov_b32 m0, s50
	s_nop 0
	global_load_lds_dwordx4 v132, s[84:85]
	s_waitcnt vmcnt(8)
	s_waitcnt lgkmcnt(0)
	s_barrier
	s_setprio 1
	s_waitcnt lgkmcnt(0)
	v_mfma_f32_16x16x32_bf16 v[62:65], v[142:145], v[184:187], v[62:65]
	v_mfma_f32_16x16x32_bf16 v[58:61], v[158:161], v[184:187], v[58:61]
	v_mfma_f32_16x16x32_bf16 v[50:53], v[142:145], v[192:195], v[50:53]
	v_mfma_f32_16x16x32_bf16 v[42:45], v[158:161], v[192:195], v[42:45]
	v_mfma_f32_16x16x32_bf16 v[34:37], v[142:145], v[200:203], v[34:37]
	v_mfma_f32_16x16x32_bf16 v[26:29], v[158:161], v[200:203], v[26:29]
	v_mfma_f32_16x16x32_bf16 v[14:17], v[142:145], v[208:211], v[14:17]
	v_mfma_f32_16x16x32_bf16 v[10:13], v[158:161], v[208:211], v[10:13]
	v_mfma_f32_16x16x32_bf16 v[62:65], v[154:157], v[188:191], v[62:65]
	v_mfma_f32_16x16x32_bf16 v[58:61], v[162:165], v[188:191], v[58:61]
	v_mfma_f32_16x16x32_bf16 v[50:53], v[154:157], v[196:199], v[50:53]
	v_mfma_f32_16x16x32_bf16 v[42:45], v[162:165], v[196:199], v[42:45]
	v_mfma_f32_16x16x32_bf16 v[34:37], v[154:157], v[204:207], v[34:37]
	v_mfma_f32_16x16x32_bf16 v[26:29], v[162:165], v[204:207], v[26:29]
	v_mfma_f32_16x16x32_bf16 v[14:17], v[154:157], v[212:215], v[14:17]
	v_mfma_f32_16x16x32_bf16 v[10:13], v[162:165], v[212:215], v[10:13]
	v_mfma_f32_16x16x32_bf16 v[54:57], v[166:169], v[184:187], v[54:57]
	v_mfma_f32_16x16x32_bf16 v[46:49], v[174:177], v[184:187], v[46:49]
	v_mfma_f32_16x16x32_bf16 v[38:41], v[166:169], v[192:195], v[38:41]
	v_mfma_f32_16x16x32_bf16 v[30:33], v[174:177], v[192:195], v[30:33]
	v_mfma_f32_16x16x32_bf16 v[22:25], v[166:169], v[200:203], v[22:25]
	v_mfma_f32_16x16x32_bf16 v[18:21], v[174:177], v[200:203], v[18:21]
	v_mfma_f32_16x16x32_bf16 v[6:9], v[166:169], v[208:211], v[6:9]
	v_mfma_f32_16x16x32_bf16 v[2:5], v[174:177], v[208:211], v[2:5]
	v_mfma_f32_16x16x32_bf16 v[54:57], v[170:173], v[188:191], v[54:57]
	v_mfma_f32_16x16x32_bf16 v[46:49], v[178:181], v[188:191], v[46:49]
	v_mfma_f32_16x16x32_bf16 v[38:41], v[170:173], v[196:199], v[38:41]
	v_mfma_f32_16x16x32_bf16 v[30:33], v[178:181], v[196:199], v[30:33]
	v_mfma_f32_16x16x32_bf16 v[22:25], v[170:173], v[204:207], v[22:25]
	v_mfma_f32_16x16x32_bf16 v[18:21], v[178:181], v[204:207], v[18:21]
	v_mfma_f32_16x16x32_bf16 v[6:9], v[170:173], v[212:215], v[6:9]
	v_mfma_f32_16x16x32_bf16 v[2:5], v[178:181], v[212:215], v[2:5]
	s_setprio 0
	s_barrier
	s_add_i32 s61, s61, 2
	s_add_u32 s30, s30, 0x100
	s_addc_u32 s31, s31, 0
	s_add_u32 s59, s59, 0x100
	s_addc_u32 s60, s60, 0
	s_cmp_gt_u32 s61, 61
	s_cbranch_scc0 .LBB0_707
	s_and_b64 vcc, exec, s[14:15]
	s_cbranch_vccz .LBB0_710
	s_barrier
